# P7: dropped the vmcnt(0) at the router->drain and drain->router transitions (stores of the previous step need not complete; LDS reuse is covered by the barrier + lgkmcnt)
# baseline (speedup 1.0000x reference)
; #define LAS __attribute__((address_space(3)))
; __device__ __forceinline__ void router_block(const Ctx& c, int blk, const float* __restrict__ h1, const float* __restrict__ g_ffn, const float* __restrict__ Wrt, const float* __restrict__ b_r, ...
;     LAS float* As = (LAS float*)(c.lds + RA_OFF); LAS float* Bs = (LAS float*)(c.lds + RB_OFF); LAS float* srstd = (LAS float*)(c.lds + RC_OFF);
;     LAS float* part = As;
;     const int lane = c.lane, m0 = blk * 32;
;     f32x4 v[4][8];
; #pragma unroll
;     for (int r = 0; r < 4; ++r) { const float* src = h1 + (size_t)(m0 + c.wave * 4 + r) * D;
; #pragma unroll
;         for (int j = 0; j < 8; ++j) v[r][j] = *(const f32x4*)(src + j * 256 + lane * 4); }
; __device__ __forceinline__ void phase7() { const Ctx c = make_ctx(); PHASE_PTRS;
;     ...
;     for (int blk = c.wg; blk < M / 32; blk += c.G) router_block(c, blk, h1, INP(12), Wrt, INP(14), xn, cnt, rowtok, tok_e, tok_p, gate);
.LBB0_1222:
	s_cmpk_gt_i32 s2, 0xff
	s_cbranch_scc1 .LBB0_1311
	v_mov_b32_e32 v165, 0
	s_nop 0
	v_lshlrev_b32_e32 v2, 4, v1
	v_mov_b32_e32 v3, v165
	v_lshl_add_u64 v[4:5], s[36:37], 0, v[2:3]
	s_mov_b64 s[8:9], 0x41e00000
	v_lshl_add_u64 v[166:167], v[4:5], 0, s[8:9]
	v_mbcnt_lo_u32_b32 v4, -1, 0
	v_mbcnt_hi_u32_b32 v4, -1, v4
	s_add_u32 s6, s36, 0x3b400000
	v_and_b32_e32 v5, 64, v4
	s_addc_u32 s7, s37, 0
	v_add_u32_e32 v5, 64, v5
	v_xor_b32_e32 v6, 1, v4
	s_add_u32 s31, s36, 0x47e00000
	v_cmp_lt_i32_e32 vcc, v6, v5
	s_addc_u32 s58, s37, 0
	s_add_u32 s59, s36, 0x47f00000
	v_cndmask_b32_e32 v6, v4, v6, vcc
	v_lshlrev_b32_e32 v163, 2, v6
	v_xor_b32_e32 v6, 2, v4
	s_addc_u32 s60, s37, 0
	v_cmp_lt_i32_e32 vcc, v6, v5
	s_add_u32 s61, s36, 0x48000000
	s_addc_u32 s62, s37, 0
	v_cndmask_b32_e32 v6, v4, v6, vcc
	v_lshlrev_b32_e32 v217, 2, v6
	v_xor_b32_e32 v6, 4, v4
	s_add_u32 s12, s36, 0x48100000
	v_cmp_lt_i32_e32 vcc, v6, v5
	s_addc_u32 s13, s37, 0
	s_lshl_b32 s10, s56, 2
	v_cndmask_b32_e32 v6, v4, v6, vcc
	v_lshlrev_b32_e32 v218, 2, v6
	v_xor_b32_e32 v6, 8, v4
	s_or_b32 s16, s10, 1
	s_load_dwordx2 s[4:5], s[34:35], 0x60
	s_load_dwordx2 s[14:15], s[34:35], 0x70
	v_cmp_lt_i32_e32 vcc, v6, v5
	s_ashr_i32 s11, s10, 31
	s_ashr_i32 s17, s16, 31
	s_or_b32 s40, s10, 2
	s_or_b32 s42, s10, 3
	v_cndmask_b32_e32 v6, v4, v6, vcc
	s_lshl_b64 s[8:9], s[10:11], 13
	s_lshl_b64 s[18:19], s[16:17], 13
	s_ashr_i32 s41, s40, 31
	s_ashr_i32 s43, s42, 31
	s_add_i32 s11, 0, 0x10200
	s_mul_i32 s17, s56, 0x2040
	v_lshlrev_b32_e32 v219, 2, v6
	v_xor_b32_e32 v6, 16, v4
	s_lshl_b32 s63, s56, 4
	s_lshl_b64 s[20:21], s[40:41], 13
	s_lshl_b64 s[24:25], s[42:43], 13
	s_add_i32 s26, s17, 0
	s_add_i32 s17, s11, s17
	v_cmp_lt_i32_e32 vcc, v6, v5
	v_add_u32_e32 v222, s26, v2
	s_add_u32 s26, s6, s24
	s_waitcnt lgkmcnt(0)
	v_lshl_add_u64 v[168:169], s[4:5], 0, v[2:3]
	s_mov_b64 s[4:5], 0x1000
	v_cndmask_b32_e32 v6, v4, v6, vcc
	s_addc_u32 s27, s7, s25
	v_lshl_add_u64 v[170:171], v[168:169], 0, s[4:5]
	s_mov_b64 s[4:5], 0x1400
	v_lshlrev_b32_e32 v220, 2, v6
	v_xor_b32_e32 v6, 32, v4
	v_lshl_add_u64 v[188:189], s[26:27], 0, v[2:3]
	s_add_u32 s26, s6, s20
	v_lshl_add_u64 v[172:173], v[168:169], 0, s[4:5]
	s_mov_b64 s[4:5], 0x1800
	v_cmp_lt_i32_e32 vcc, v6, v5
	s_addc_u32 s27, s7, s21
	v_lshlrev_b32_e32 v164, 2, v1
	v_lshl_add_u64 v[174:175], v[168:169], 0, s[4:5]
	s_mov_b64 s[4:5], 0x1c00
	v_cndmask_b32_e32 v4, v4, v6, vcc
	v_lshl_add_u64 v[190:191], s[26:27], 0, v[2:3]
	s_add_u32 s26, s6, s18
	v_lshl_add_u64 v[176:177], v[168:169], 0, s[4:5]
	v_lshlrev_b32_e32 v221, 2, v4
	v_lshl_add_u64 v[4:5], s[36:37], 0, v[164:165]
	s_mov_b64 s[4:5], 0x45e00000
	s_addc_u32 s27, s7, s19
	v_lshl_add_u64 v[178:179], v[4:5], 0, s[4:5]
	v_lshl_add_u64 v[4:5], s[6:7], 0, v[2:3]
	s_add_u32 s6, s6, s8
	v_lshl_add_u64 v[180:181], v[4:5], 0, s[8:9]
	v_lshl_add_u64 v[182:183], v[4:5], 0, s[18:19]
	v_lshl_add_u64 v[184:185], v[4:5], 0, s[20:21]
	v_lshl_add_u64 v[186:187], v[4:5], 0, s[24:25]
	v_and_b32_e32 v4, 15, v216
	v_lshrrev_b32_e32 v5, 2, v216
	s_addc_u32 s7, s7, s9
	v_and_b32_e32 v5, 12, v5
	v_mul_u32_u24_e32 v6, 0x204, v4
	v_lshl_add_u64 v[194:195], s[6:7], 0, v[2:3]
	s_and_b32 s6, s44, 0x3fffffc0
	v_lshlrev_b32_e32 v6, 2, v6
	v_or_b32_e32 v8, s6, v5
	v_add_u32_e32 v7, 0x8100, v6
	v_lshlrev_b32_e32 v8, 2, v8
	v_add_u32_e32 v9, s11, v8
	v_add3_u32 v227, s11, v7, v8
	s_add_u32 s11, s36, 0x3b400800
	v_add_u32_e32 v223, s17, v2
	s_addc_u32 s17, s37, 0
	s_add_u32 s6, s11, s24
	s_addc_u32 s7, s17, s25
	v_lshl_add_u64 v[196:197], s[6:7], 0, v[2:3]
	s_add_u32 s6, s11, s20
	s_addc_u32 s7, s17, s21
	v_lshl_add_u64 v[198:199], s[6:7], 0, v[2:3]
	s_add_u32 s6, s11, s18
	s_addc_u32 s7, s17, s19
	v_lshl_add_u64 v[200:201], s[6:7], 0, v[2:3]
	s_add_u32 s6, s11, s8
	s_addc_u32 s7, s17, s9
	s_add_u32 s11, s36, 0x3b401000
	s_addc_u32 s17, s37, 0
	v_lshl_add_u64 v[202:203], s[6:7], 0, v[2:3]
	s_add_u32 s6, s11, s24
	s_addc_u32 s7, s17, s25
	v_lshl_add_u64 v[204:205], s[6:7], 0, v[2:3]
	s_add_u32 s6, s11, s20
	s_addc_u32 s7, s17, s21
	v_lshl_add_u64 v[206:207], s[6:7], 0, v[2:3]
	s_add_u32 s6, s11, s18
	s_addc_u32 s7, s17, s19
	v_lshl_add_u64 v[208:209], s[6:7], 0, v[2:3]
	s_add_u32 s6, s11, s8
	s_addc_u32 s7, s17, s9
	s_add_i32 s70, 0, 0x20400
	s_lshl_b32 s11, s16, 2
	s_add_i32 s66, s70, s11
	s_lshl_b32 s11, s40, 2
	s_add_i32 s68, s70, s11
	s_lshl_b32 s11, s42, 2
	v_lshl_add_u64 v[192:193], s[26:27], 0, v[2:3]
	v_lshl_add_u64 v[210:211], s[6:7], 0, v[2:3]
	s_lshl_b32 s6, s56, 12
	s_add_i32 s70, s70, s11
	v_lshlrev_b32_e32 v2, 5, v216
	s_lshl_b32 s11, s2, 5
	v_add3_u32 v224, 0, v6, v8
	v_add_u32_e32 v225, v9, v6
	v_lshl_add_u32 v4, v4, 2, 0
	v_lshl_or_b32 v5, v5, 7, s6
	v_lshlrev_b32_e32 v6, 2, v216
	s_add_i32 s8, 0, 0x20480
	v_lshl_add_u64 v[212:213], s[14:15], 0, v[164:165]
	v_ashrrev_i32_e32 v3, 31, v2
	s_add_i32 s71, 0, 0x20500
	s_add_i32 s14, s11, s10
	s_lshl_b32 s10, s2, 7
	v_cmp_eq_u32_e64 s[4:5], 0, v1
	v_add_u32_e32 v226, v9, v7
	v_cmp_gt_i32_e64 s[6:7], 32, v216
	v_add_u32_e32 v228, s8, v6
	v_cmp_gt_u32_e64 s[8:9], 32, v1
	v_add_u32_e32 v229, 0, v164
	s_lshl_b32 s64, s56, 9
	s_lshl_b32 s65, s16, 7
	s_lshl_b32 s67, s40, 7
	s_lshl_b32 s69, s42, 7
	v_lshl_add_u64 v[214:215], v[2:3], 2, s[36:37]
	v_add_u32_e32 v230, s71, v6
	s_lshl_b32 s72, s3, 5
	s_add_i32 s16, s10, s63
	s_lshl_b32 s73, s3, 7
	s_movk_i32 s74, 0x1000
	v_mov_b32_e32 v231, 0x358637bd
	s_mov_b32 s75, 0x800000
	v_add_u32_e32 v232, v4, v5
	s_mov_b32 s76, 0x3fb8aa3b
	s_mov_b32 s77, 0xc2ce8ed0
	s_mov_b32 s78, 0x42b17218
	v_mov_b32_e32 v233, 0xff800000
	v_mov_b32_e32 v234, 0x7f800000
	s_mov_b32 s79, s2
	s_branch .LBB0_1225

; #define LAS __attribute__((address_space(3)))
; __device__ __forceinline__ void drain_balanced(const Ctx& c, const unsigned* ctl, const float* w_gu, const float* w_d, unsigned char* Wgu, unsigned char* Wd) {
;     LAS int* pre = (LAS int*)(c.lds + DR_OFF); LAS int* prog = pre + 1025; LAS int* wt = prog + 1024;
;     __syncthreads();
;     int n0 = (int)ctl[CW_PROG + 2 * c.tid], n1 = (int)ctl[CW_PROG + 2 * c.tid + 1];
;     const int N0 = (CONV_TOTAL - 2 * c.tid + CONV_SLOTS - 1) / CONV_SLOTS, N1 = (CONV_TOTAL - (2 * c.tid + 1) + CONV_SLOTS - 1) / CONV_SLOTS;
;     const int l0 = N0 > n0 ? N0 - n0 : 0, l1 = N1 > n1 ? N1 - n1 : 0;
;     int incl = l0 + l1;
; #pragma unroll
;     for (int o = 1; o < 64; o <<= 1) { const int v = __shfl_up(incl, o); if (c.lane >= o) incl += v; }
;     if (c.lane == 63) wt[c.wave] = incl;
;     prog[2 * c.tid] = n0; prog[2 * c.tid + 1] = n1;
;     __syncthreads();
;     int base = 0, total = 0;
; #pragma unroll
;     for (int w = 0; w < NWAVES; ++w) { const int t = wt[w]; base += (w < c.wave) ? t : 0; total += t; }
;     const int excl = base + incl - (l0 + l1);
;     pre[2 * c.tid] = excl; pre[2 * c.tid + 1] = excl + l0;
;     if (c.tid == 0) pre[1024] = total;
; __device__ __forceinline__ void phase7() { const Ctx c = make_ctx(); PHASE_PTRS;
;     ...
;     if (!drain_first) drain_balanced(c, ctl7, INP(15), INP(17), (unsigned char*)Wgu, (unsigned char*)Wd);
.LBB0_1311:
	s_and_b64 vcc, exec, s[38:39]
	s_cbranch_vccz .LBB0_1363
	v_ashrrev_i32_e32 v163, 31, v162
	s_nop 0
	v_lshl_add_u64 v[2:3], v[162:163], 2, s[36:37]
	v_add_co_u32_e32 v2, vcc, 0x2000, v2
	s_nop 1
	v_addc_co_u32_e32 v3, vcc, 0, v3, vcc
	s_barrier
	global_load_dwordx2 v[2:3], v[2:3], off
	v_sub_u32_e32 v4, 0x183ff, v162
	v_sub_u32_e32 v5, 0x183fe, v162
	v_mbcnt_lo_u32_b32 v6, -1, 0
	v_ashrrev_i32_e32 v7, 31, v4
	v_ashrrev_i32_e32 v8, 31, v5
	v_mbcnt_hi_u32_b32 v6, -1, v6
	v_lshrrev_b32_e32 v7, 22, v7
	v_lshrrev_b32_e32 v8, 22, v8
	v_and_b32_e32 v9, 64, v6
	v_add_u32_e32 v10, -1, v6
	v_add_u32_e32 v4, v4, v7
	v_add_u32_e32 v5, v5, v8
	v_cmp_lt_i32_e32 vcc, v10, v9
	v_ashrrev_i32_e32 v4, 10, v4
	v_ashrrev_i32_e32 v5, 10, v5
	v_cndmask_b32_e32 v7, v10, v6, vcc
	v_lshlrev_b32_e32 v7, 2, v7
	v_add_u32_e32 v11, -2, v6
	v_add_u32_e32 v12, -4, v6
	v_add_u32_e32 v13, -8, v6
	v_add_u32_e32 v14, -16, v6
	v_subrev_u32_e32 v15, 32, v6
	s_waitcnt vmcnt(0)
	v_sub_u32_e32 v8, v4, v2
	v_cmp_gt_i32_e32 vcc, v4, v2
	v_sub_u32_e32 v10, v5, v3
	s_nop 0
	v_cndmask_b32_e32 v4, 0, v8, vcc
	v_cmp_gt_i32_e32 vcc, v5, v3
	s_nop 1
	v_cndmask_b32_e32 v5, 0, v10, vcc
	v_add_u32_e32 v5, v5, v4
	ds_bpermute_b32 v7, v7, v5
	v_cmp_lt_i32_e32 vcc, v11, v9
	s_nop 1
	v_cndmask_b32_e32 v8, v11, v6, vcc
	v_cmp_ne_u32_e32 vcc, 0, v1
	v_lshlrev_b32_e32 v8, 2, v8
	s_waitcnt lgkmcnt(0)
	v_cndmask_b32_e32 v7, 0, v7, vcc
	v_add_u32_e32 v7, v7, v5
	ds_bpermute_b32 v8, v8, v7
	v_cmp_lt_i32_e32 vcc, v12, v9
	s_nop 1
	v_cndmask_b32_e32 v10, v12, v6, vcc
	v_cmp_lt_u32_e32 vcc, 1, v1
	v_lshlrev_b32_e32 v10, 2, v10
	s_waitcnt lgkmcnt(0)
	v_cndmask_b32_e32 v8, 0, v8, vcc
	v_add_u32_e32 v7, v8, v7
	ds_bpermute_b32 v8, v10, v7
	v_cmp_lt_i32_e32 vcc, v13, v9
	s_nop 1
	v_cndmask_b32_e32 v10, v13, v6, vcc
	v_cmp_lt_u32_e32 vcc, 3, v1
	v_lshlrev_b32_e32 v10, 2, v10
	s_waitcnt lgkmcnt(0)
	v_cndmask_b32_e32 v8, 0, v8, vcc
	v_add_u32_e32 v7, v8, v7
	ds_bpermute_b32 v8, v10, v7
	v_cmp_lt_i32_e32 vcc, v14, v9
	s_nop 1
	v_cndmask_b32_e32 v10, v14, v6, vcc
	v_cmp_lt_u32_e32 vcc, 7, v1
	v_lshlrev_b32_e32 v10, 2, v10
	s_waitcnt lgkmcnt(0)
	v_cndmask_b32_e32 v8, 0, v8, vcc
	v_add_u32_e32 v7, v8, v7
	ds_bpermute_b32 v8, v10, v7
	v_cmp_lt_i32_e32 vcc, v15, v9
	s_nop 1
	v_cndmask_b32_e32 v6, v15, v6, vcc
	v_cmp_lt_u32_e32 vcc, 15, v1
	v_lshlrev_b32_e32 v6, 2, v6
	s_waitcnt lgkmcnt(0)
	v_cndmask_b32_e32 v8, 0, v8, vcc
	v_add_u32_e32 v7, v8, v7
	ds_bpermute_b32 v6, v6, v7
	v_cmp_lt_u32_e32 vcc, 31, v1
	s_waitcnt lgkmcnt(0)
	s_nop 0
	v_cndmask_b32_e32 v6, 0, v6, vcc
	v_add_u32_e32 v6, v6, v7
	v_cmp_eq_u32_e32 vcc, 63, v1
	s_and_saveexec_b64 s[4:5], vcc
	s_lshl_b32 s6, s56, 2
	s_add_i32 s6, s6, 0
	s_add_i32 s6, s6, 0x23004
	v_mov_b32_e32 v7, s6
	ds_write_b32 v7, v6
	s_or_b64 exec, exec, s[4:5]
	v_lshl_add_u32 v7, v216, 3, 0
	v_add_u32_e32 v8, 0x22004, v7
	s_add_i32 s8, 0, 0x23004
	s_load_dwordx2 s[4:5], s[34:35], 0x78
	s_load_dwordx2 s[6:7], s[34:35], 0x88
	ds_write2_b32 v8, v2, v3 offset1:1
	v_mov_b32_e32 v2, s8
	s_waitcnt lgkmcnt(0)
	s_barrier
	ds_read2_b32 v[2:3], v2 offset1:1
	s_cmp_gt_i32 s56, 0
	v_cmp_eq_u32_e32 vcc, 0, v216
	s_waitcnt lgkmcnt(0)
	v_readfirstlane_b32 s8, v2
	v_readfirstlane_b32 s9, v3
	s_cselect_b32 s10, s8, 0
	s_cmp_gt_i32 s56, 1
	s_cselect_b32 s11, s9, 0
	s_add_i32 s12, 0, 0x2300c
	v_mov_b32_e32 v2, s12
	ds_read2_b32 v[2:3], v2 offset1:1
	s_add_i32 s8, s9, s8
	s_cmp_gt_i32 s56, 2
	s_waitcnt lgkmcnt(0)
	v_readfirstlane_b32 s9, v2
	s_cselect_b32 s13, s9, 0
	s_add_i32 s8, s8, s9
	v_readfirstlane_b32 s12, v3
	s_cmp_gt_i32 s56, 3
	s_cselect_b32 s9, s12, 0
	s_add_i32 s14, 0, 0x23014
	v_mov_b32_e32 v2, s14
	ds_read2_b32 v[2:3], v2 offset1:1
	s_add_i32 s8, s8, s12
	s_cmp_gt_i32 s56, 4
	s_waitcnt lgkmcnt(0)
	v_readfirstlane_b32 s12, v2
	s_cselect_b32 s15, s12, 0
	s_add_i32 s8, s8, s12
	v_readfirstlane_b32 s14, v3
	s_cmp_gt_i32 s56, 5
	s_cselect_b32 s12, s14, 0
	s_add_i32 s16, 0, 0x2301c
	v_mov_b32_e32 v2, s16
	ds_read2_b32 v[2:3], v2 offset1:1
	s_add_i32 s8, s8, s14
	s_cmp_gt_i32 s56, 6
	s_waitcnt lgkmcnt(0)
	v_readfirstlane_b32 s14, v2
	s_cselect_b32 s17, s14, 0
	s_add_i32 s8, s8, s14
	v_readfirstlane_b32 s16, v3
	s_cmp_gt_i32 s56, 7
	s_cselect_b32 s14, s16, 0
	s_add_i32 s16, s8, s16
	s_add_i32 s8, s14, s17
	s_add_i32 s8, s8, s12
	s_add_i32 s8, s8, s15
	s_add_i32 s8, s8, s9
	s_add_i32 s8, s8, s13
	s_add_i32 s8, s8, s11
	v_sub_u32_e32 v2, v6, v5
	s_add_i32 s8, s8, s10
	v_add_u32_e32 v2, s8, v2
	v_add_u32_e32 v5, 0x21000, v7
	v_add_u32_e32 v3, v2, v4
	ds_write_b64 v5, v[2:3]
	s_and_saveexec_b64 s[8:9], vcc
	s_add_i32 s10, 0, 0x22000
	v_mov_b32_e32 v2, s10
	v_mov_b32_e32 v3, s16
	ds_write_b32 v2, v3
	s_or_b64 exec, exec, s[8:9]
	s_mul_hi_i32 s9, s16, s57
	s_mul_i32 s8, s16, s57
	s_ashr_i32 s31, s30, 31
	s_or_b64 s[10:11], s[8:9], s[30:31]
	s_mov_b32 s10, 0
	s_cmp_lg_u64 s[10:11], 0
	s_waitcnt lgkmcnt(0)
	s_barrier
; __device__ __forceinline__ void drain_balanced(const Ctx& c, const unsigned* ctl, const float* w_gu, const float* w_d, unsigned char* Wgu, unsigned char* Wd) {
;     ...
;     const int lo = __builtin_amdgcn_readfirstlane((int)((long long)c.gw * total / c.NGW)), hi = __builtin_amdgcn_readfirstlane((int)((long long)(c.gw + 1) * total / c.NGW));
	s_cbranch_scc0 .LBB0_1328
	s_ashr_i32 s12, s31, 31
	s_add_u32 s10, s30, s12
	s_mov_b32 s13, s12
	s_addc_u32 s11, s31, s12
	s_xor_b64 s[14:15], s[10:11], s[12:13]
	v_cvt_f32_u32_e32 v2, s14
	v_cvt_f32_u32_e32 v3, s15
	s_sub_u32 s17, 0, s14
	s_subb_u32 s20, 0, s15
	v_fmamk_f32 v2, v3, 0x4f800000, v2
	v_rcp_f32_e32 v2, v2
	s_nop 0
	v_mul_f32_e32 v2, 0x5f7ffffc, v2
	v_mul_f32_e32 v3, 0x2f800000, v2
	v_trunc_f32_e32 v3, v3
	v_fmamk_f32 v2, v3, 0xcf800000, v2
	v_cvt_u32_f32_e32 v3, v3
	v_cvt_u32_f32_e32 v2, v2
	v_readfirstlane_b32 s21, v3
	v_readfirstlane_b32 s18, v2
	s_mul_i32 s19, s17, s21
	s_mul_hi_u32 s25, s17, s18
	s_mul_i32 s24, s20, s18
	s_add_i32 s19, s25, s19
	s_add_i32 s19, s19, s24
	s_mul_i32 s26, s17, s18
	s_mul_i32 s25, s18, s19
	s_mul_hi_u32 s27, s18, s26
	s_mul_hi_u32 s24, s18, s19
	s_add_u32 s25, s27, s25
	s_addc_u32 s24, 0, s24
	s_mul_hi_u32 s34, s21, s26
	s_mul_i32 s26, s21, s26
	s_add_u32 s25, s25, s26
	s_mul_hi_u32 s27, s21, s19
	s_addc_u32 s24, s24, s34
	s_addc_u32 s25, s27, 0
	s_mul_i32 s19, s21, s19
	s_add_u32 s19, s24, s19
	s_addc_u32 s24, 0, s25
	s_add_u32 s25, s18, s19
	s_cselect_b64 s[18:19], -1, 0
	s_cmp_lg_u64 s[18:19], 0
	s_addc_u32 s21, s21, s24
	s_mul_i32 s18, s17, s21
	s_mul_hi_u32 s19, s17, s25
	s_add_i32 s18, s19, s18
	s_mul_i32 s20, s20, s25
	s_add_i32 s18, s18, s20
	s_mul_i32 s17, s17, s25
	s_mul_hi_u32 s20, s21, s17
	s_mul_i32 s24, s21, s17
	s_mul_i32 s27, s25, s18
	s_mul_hi_u32 s17, s25, s17
	s_mul_hi_u32 s26, s25, s18
	s_add_u32 s17, s17, s27
	s_addc_u32 s26, 0, s26
	s_add_u32 s17, s17, s24
	s_mul_hi_u32 s19, s21, s18
	s_addc_u32 s17, s26, s20
	s_addc_u32 s19, s19, 0
	s_mul_i32 s18, s21, s18
	s_add_u32 s17, s17, s18
	s_addc_u32 s20, 0, s19
	s_add_u32 s17, s25, s17
	s_cselect_b64 s[18:19], -1, 0
	s_cmp_lg_u64 s[18:19], 0
	s_addc_u32 s24, s21, s20
	s_ashr_i32 s18, s9, 31
	s_add_u32 s20, s8, s18
	s_mov_b32 s19, s18
	s_addc_u32 s21, s9, s18
	s_xor_b64 s[20:21], s[20:21], s[18:19]
	s_mul_i32 s25, s20, s24
	s_mul_hi_u32 s26, s20, s17
	s_mul_hi_u32 s9, s20, s24
	s_add_u32 s25, s26, s25
	s_addc_u32 s9, 0, s9
	s_mul_hi_u32 s27, s21, s17
	s_mul_i32 s17, s21, s17
	s_add_u32 s17, s25, s17
	s_mul_hi_u32 s26, s21, s24
	s_addc_u32 s9, s9, s27
	s_addc_u32 s17, s26, 0
	s_mul_i32 s24, s21, s24
	s_add_u32 s9, s9, s24
	s_addc_u32 s17, 0, s17
	s_mul_i32 s24, s14, s17
	s_mul_hi_u32 s25, s14, s9
	s_add_i32 s24, s25, s24
	s_mul_i32 s25, s15, s9
	s_add_i32 s34, s24, s25
	s_sub_i32 s26, s21, s34
	s_mul_i32 s24, s14, s9
	s_sub_u32 s20, s20, s24
	s_cselect_b64 s[24:25], -1, 0
	s_cmp_lg_u64 s[24:25], 0
	s_subb_u32 s35, s26, s15
	s_sub_u32 s36, s20, s14
	s_cselect_b64 s[26:27], -1, 0
	s_cmp_lg_u64 s[26:27], 0
	s_subb_u32 s26, s35, 0
	s_cmp_ge_u32 s26, s15
	s_cselect_b32 s27, -1, 0
	s_cmp_ge_u32 s36, s14
	s_cselect_b32 s35, -1, 0
	s_cmp_eq_u32 s26, s15
	s_cselect_b32 s26, s35, s27
	s_add_u32 s27, s9, 1
	s_addc_u32 s35, s17, 0
	s_add_u32 s36, s9, 2
	s_addc_u32 s37, s17, 0
	s_cmp_lg_u32 s26, 0
	s_cselect_b32 s26, s36, s27
	s_cselect_b32 s27, s37, s35
	s_cmp_lg_u64 s[24:25], 0
	s_subb_u32 s21, s21, s34
	s_cmp_ge_u32 s21, s15
	s_cselect_b32 s24, -1, 0
	s_cmp_ge_u32 s20, s14
	s_cselect_b32 s14, -1, 0
	s_cmp_eq_u32 s21, s15
	s_cselect_b32 s14, s14, s24
	s_cmp_lg_u32 s14, 0
	s_cselect_b32 s15, s27, s17
	s_cselect_b32 s14, s26, s9
	s_xor_b64 s[12:13], s[18:19], s[12:13]
	s_xor_b64 s[14:15], s[14:15], s[12:13]
	s_sub_u32 s12, s14, s12
	s_subb_u32 s13, s15, s13
	v_cvt_f32_u32_e32 v4, s30
	v_mov_b64_e32 v[2:3], s[12:13]
	s_cbranch_execnz .LBB0_1319
